# waves 0-3 run their epilogue + unit switch (critical path at a unit boundary) at priority 2, back to 0 before the K-loop
# baseline (speedup 1.0000x reference)
; template <class Epi, class Sched>
; __device__ __forceinline__ void gemm_phase(LAS unsigned char* lds, const bf16_t* Abase, const int K, const Sched& S, const Epi& E, const int wvid) {
;     ...
; #pragma unroll
;         for (int a = 0; a < 2; ++a)
; #pragma unroll
;             for (int b = 0; b < 2; ++b)
; #pragma unroll
;                 for (int m = 0; m < 4; ++m)
; #pragma unroll
;                     for (int n = 0; n < 2; ++n) acc[a][b][m][n] = (f32x4){0.f, 0.f, 0.f, 0.f};
.LBB0_124:
	s_ashr_i32 s25, s24, 31
	s_lshl_b64 s[26:27], s[24:25], 19
	s_add_u32 s26, s38, s26
	s_addc_u32 s27, s39, s27
	s_and_b64 s[28:29], s[0:1], exec
	s_cselect_b32 s25, s27, s5
	s_cselect_b32 s58, s26, s4
	s_add_u32 s59, s4, 0x100
	v_mov_b32_e32 v2, 0
	s_addc_u32 s60, s5, 0
	s_mov_b32 s61, -2
	s_mov_b64 s[4:5], 0
	v_mov_b32_e32 v3, v2
	v_mov_b64_e32 v[4:5], 0
	v_mov_b64_e32 v[6:7], 0
	v_mov_b64_e32 v[8:9], 0
	v_mov_b64_e32 v[18:19], 0
	v_mov_b64_e32 v[20:21], 0
	v_mov_b64_e32 v[22:23], 0
	v_mov_b64_e32 v[24:25], 0
	v_mov_b64_e32 v[34:35], 0
	v_mov_b64_e32 v[36:37], 0
	v_mov_b64_e32 v[38:39], 0
	v_mov_b64_e32 v[40:41], 0
	v_mov_b64_e32 v[50:51], 0
	v_mov_b64_e32 v[52:53], 0
	v_mov_b64_e32 v[54:55], 0
	v_mov_b64_e32 v[56:57], 0
	v_mov_b64_e32 v[10:11], 0
	v_mov_b64_e32 v[12:13], 0
	v_mov_b64_e32 v[14:15], 0
	v_mov_b64_e32 v[16:17], 0
	v_mov_b64_e32 v[26:27], 0
	v_mov_b64_e32 v[28:29], 0
	v_mov_b64_e32 v[30:31], 0
	v_mov_b64_e32 v[32:33], 0
	v_mov_b64_e32 v[42:43], 0
	v_mov_b64_e32 v[44:45], 0
	v_mov_b64_e32 v[46:47], 0
	v_mov_b64_e32 v[48:49], 0
	v_mov_b64_e32 v[58:59], 0
	v_mov_b64_e32 v[60:61], 0
	v_mov_b64_e32 v[62:63], 0
	v_mov_b64_e32 v[64:65], 0
	v_mov_b64_e32 v[66:67], 0
	v_mov_b64_e32 v[68:69], 0
	v_mov_b64_e32 v[70:71], 0
	v_mov_b64_e32 v[72:73], 0
	v_mov_b64_e32 v[74:75], 0
	v_mov_b64_e32 v[76:77], 0
	v_mov_b64_e32 v[78:79], 0
	v_mov_b64_e32 v[80:81], 0
	v_mov_b64_e32 v[90:91], 0
	v_mov_b64_e32 v[92:93], 0
	v_mov_b64_e32 v[94:95], 0
	v_mov_b64_e32 v[96:97], 0
	v_mov_b64_e32 v[106:107], 0
	v_mov_b64_e32 v[108:109], 0
	v_mov_b64_e32 v[110:111], 0
	v_mov_b64_e32 v[112:113], 0
	v_mov_b64_e32 v[82:83], 0
	v_mov_b64_e32 v[84:85], 0
	v_mov_b64_e32 v[86:87], 0
	v_mov_b64_e32 v[88:89], 0
	v_mov_b64_e32 v[98:99], 0
	v_mov_b64_e32 v[100:101], 0
	v_mov_b64_e32 v[102:103], 0
	v_mov_b64_e32 v[104:105], 0
	v_mov_b64_e32 v[114:115], 0
	v_mov_b64_e32 v[116:117], 0
	v_mov_b64_e32 v[118:119], 0
	v_mov_b64_e32 v[120:121], 0
	v_mov_b64_e32 v[122:123], 0
	v_mov_b64_e32 v[124:125], 0
	v_mov_b64_e32 v[126:127], 0
	v_mov_b64_e32 v[128:129], 0
	s_cmp_lt_u32 s74, 0x100
	s_cbranch_scc0 .Lzb0
	s_setprio 0
	s_branch .Lz0
.Lzb0:
	s_cmp_eq_u32 s100, 0
	s_cbranch_scc1 .Lz0
	s_barrier

; #define PG8_MMA(ai, bj, At, Bt) do { __builtin_amdgcn_s_setprio(1); _Pragma("unroll") for (int m = 0; m < 4; ++m) _Pragma("unroll") for (int n = 0; n < 2; ++n) _Pragma("unroll") for (int k = 0; k < 2; ++k) \
;         acc[ai][bj][m][n] = __builtin_amdgcn_mfma_f32_16x16x32_bf16(Bt[n][k], At[m][k], acc[ai][bj][m][n], 0, 0, 0); __builtin_amdgcn_s_setprio(0); } while (0)
; #define PG8_WAIT_V(n) asm volatile("s_waitcnt vmcnt(" #n ")" ::: "memory")
; #define PG8_BAR __builtin_amdgcn_s_barrier()
; template <class Epi, class Sched>
; __device__ __forceinline__ void gemm_phase(LAS unsigned char* lds, const bf16_t* Abase, const int K, const Sched& S, const Epi& E, const int wvid) {
;     ...
;             PG8_WAIT_V(6); PG8_BAR; PG8_MMA(1, 1, At, B1); PG8_BAR;
;         }
;         E(acc, cur, wr, wc, fr, fq);
.Lx_in:
	s_cmp_lt_u32 s74, 0x100
	s_cbranch_scc0 .LBB0_130
	s_barrier
	s_setprio 2

; template <class Epi, class Sched>
; __device__ __forceinline__ void gemm_phase(LAS unsigned char* lds, const bf16_t* Abase, const int K, const Sched& S, const Epi& E, const int wvid) {
;     ...
; #pragma unroll
;         for (int a = 0; a < 2; ++a)
; #pragma unroll
;             for (int b = 0; b < 2; ++b)
; #pragma unroll
;                 for (int m = 0; m < 4; ++m)
; #pragma unroll
;                     for (int n = 0; n < 2; ++n) acc[a][b][m][n] = (f32x4){0.f, 0.f, 0.f, 0.f};
.LBB0_1001:
	s_ashr_i32 s11, s10, 31
	s_ashr_i32 s17, s16, 31
	s_xor_b64 s[20:21], s[24:25], -1
	s_lshl_b64 s[18:19], s[10:11], 19
	s_lshl_b64 s[28:29], s[16:17], 1
	s_add_u32 s11, s38, s18
	s_addc_u32 s17, s39, s19
	s_add_u32 s18, s11, s28
	s_addc_u32 s19, s17, s29
	s_and_b64 s[28:29], s[24:25], exec
	s_cselect_b32 s11, s19, s27
	s_cselect_b32 s17, s18, s26
	s_add_u32 s23, s26, 0x100
	v_mov_b32_e32 v2, 0
	s_addc_u32 s58, s27, 0
	s_add_i32 s59, s57, -2
	s_mov_b32 s60, 0
	s_mov_b64 s[26:27], 0
	v_mov_b32_e32 v3, v2
	v_mov_b64_e32 v[4:5], 0
	v_mov_b64_e32 v[6:7], 0
	v_mov_b64_e32 v[8:9], 0
	v_mov_b64_e32 v[10:11], 0
	v_mov_b64_e32 v[12:13], 0
	v_mov_b64_e32 v[14:15], 0
	v_mov_b64_e32 v[16:17], 0
	v_mov_b64_e32 v[22:23], 0
	v_mov_b64_e32 v[24:25], 0
	v_mov_b64_e32 v[30:31], 0
	v_mov_b64_e32 v[32:33], 0
	v_mov_b64_e32 v[38:39], 0
	v_mov_b64_e32 v[40:41], 0
	v_mov_b64_e32 v[46:47], 0
	v_mov_b64_e32 v[48:49], 0
	v_mov_b64_e32 v[18:19], 0
	v_mov_b64_e32 v[20:21], 0
	v_mov_b64_e32 v[26:27], 0
	v_mov_b64_e32 v[28:29], 0
	v_mov_b64_e32 v[34:35], 0
	v_mov_b64_e32 v[36:37], 0
	v_mov_b64_e32 v[42:43], 0
	v_mov_b64_e32 v[44:45], 0
	v_mov_b64_e32 v[50:51], 0
	v_mov_b64_e32 v[52:53], 0
	v_mov_b64_e32 v[54:55], 0
	v_mov_b64_e32 v[56:57], 0
	v_mov_b64_e32 v[58:59], 0
	v_mov_b64_e32 v[60:61], 0
	v_mov_b64_e32 v[62:63], 0
	v_mov_b64_e32 v[64:65], 0
	v_mov_b64_e32 v[66:67], 0
	s_waitcnt vmcnt(0)
	v_mov_b64_e32 v[68:69], 0
	v_mov_b64_e32 v[70:71], 0
	v_mov_b64_e32 v[72:73], 0
	v_mov_b64_e32 v[74:75], 0
	v_mov_b64_e32 v[76:77], 0
	v_mov_b64_e32 v[78:79], 0
	v_mov_b64_e32 v[80:81], 0
	v_mov_b64_e32 v[82:83], 0
	v_mov_b64_e32 v[84:85], 0
	v_mov_b64_e32 v[86:87], 0
	v_mov_b64_e32 v[88:89], 0
	v_mov_b64_e32 v[90:91], 0
	v_mov_b64_e32 v[92:93], 0
	v_mov_b64_e32 v[94:95], 0
	v_mov_b64_e32 v[96:97], 0
	v_mov_b64_e32 v[98:99], 0
	v_mov_b64_e32 v[100:101], 0
	v_mov_b64_e32 v[102:103], 0
	v_mov_b64_e32 v[104:105], 0
	v_mov_b64_e32 v[106:107], 0
	v_mov_b64_e32 v[108:109], 0
	v_mov_b64_e32 v[110:111], 0
	v_mov_b64_e32 v[112:113], 0
	v_mov_b64_e32 v[114:115], 0
	v_mov_b64_e32 v[116:117], 0
	v_mov_b64_e32 v[118:119], 0
	v_mov_b64_e32 v[120:121], 0
	v_mov_b64_e32 v[122:123], 0
	v_mov_b64_e32 v[124:125], 0
	v_mov_b64_e32 v[126:127], 0
	v_mov_b64_e32 v[128:129], 0
	s_cmp_lt_u32 s74, 0x100
	s_cbranch_scc0 .Lzb1
	s_setprio 0
	s_branch .Lz1

;     __device__ __forceinline__ void operator()(const f32x4 (&acc)[2][2][4][2], const Unit& u, int wr, int wc, int fr, int fq) const {
;     ...
; #pragma unroll
;         for (int ai = 0; ai < 2; ++ai)
; #pragma unroll
;             for (int m = 0; m < 4; ++m) { const size_t ro = (size_t)(row0 + ai * HALF + m * 16) * D + col0;
; #pragma unroll
;                 for (int bj = 0; bj < 2; ++bj) { const u32x4 h = *(const u32x4*)(hb + ro + bj * HALF); const f32x4 v0 = acc[ai][bj][m][0], v1 = acc[ai][bj][m][1];
.LBB0_1007:
	v_lshl_or_b32 v130, s22, 8, v189
	s_mov_b64 s[22:23], -1
	s_cmp_lt_i32 s57, 16
	v_ashrrev_i32_e32 v131, 31, v130
	s_cbranch_scc1 .Lgo_ks
	v_add_u32_e32 v132, s9, v188
	v_ashrrev_i32_e32 v133, 31, v132
	v_lshlrev_b64 v[132:133], 10, v[132:133]
	v_lshl_add_u64 v[132:133], v[132:133], 0, v[130:131]
	v_lshlrev_b64 v[132:133], 1, v[132:133]
	v_lshl_add_u64 v[138:139], s[4:5], 0, v[132:133]
	v_lshl_add_u64 v[140:141], s[2:3], 0, v[132:133]
	v_mov_b64_e32 v[142:143], v[138:139]
	global_load_dwordx4 v[144:147], v[142:143], off
	global_load_dwordx4 v[148:151], v[142:143], off offset:256
	v_add_co_u32_e32 v142, vcc, 0x8000, v142
	s_nop 1
	v_addc_co_u32_e32 v143, vcc, 0, v143, vcc
	global_load_dwordx4 v[152:155], v[142:143], off
	global_load_dwordx4 v[156:159], v[142:143], off offset:256
	v_add_co_u32_e32 v142, vcc, 0x8000, v142
	s_nop 1
	v_addc_co_u32_e32 v143, vcc, 0, v143, vcc
	global_load_dwordx4 v[160:163], v[142:143], off
	global_load_dwordx4 v[164:167], v[142:143], off offset:256
	v_add_co_u32_e32 v142, vcc, 0x8000, v142
	s_nop 1
	v_addc_co_u32_e32 v143, vcc, 0, v143, vcc
	global_load_dwordx4 v[168:171], v[142:143], off
	global_load_dwordx4 v[172:175], v[142:143], off offset:256
	v_add_co_u32_e32 v142, vcc, 0x28000, v142
	s_nop 1
	v_addc_co_u32_e32 v143, vcc, 0, v143, vcc
	s_cmp_lt_u32 s74, 0x100
	s_cbranch_scc0 .Lxa3
	s_barrier
	s_setprio 2

; template <class Epi, class Sched>
; __device__ __forceinline__ void gemm_phase(LAS unsigned char* lds, const bf16_t* Abase, const int K, const Sched& S, const Epi& E, const int wvid) {
;     ...
; #pragma unroll
;         for (int a = 0; a < 2; ++a)
; #pragma unroll
;             for (int b = 0; b < 2; ++b)
; #pragma unroll
;                 for (int m = 0; m < 4; ++m)
; #pragma unroll
;                     for (int n = 0; n < 2; ++n) acc[a][b][m][n] = (f32x4){0.f, 0.f, 0.f, 0.f};
.LBB0_1208:
	s_ashr_i32 s23, s22, 31
	s_lshl_b64 s[4:5], s[22:23], 19
	v_ashrrev_i32_e32 v191, 31, v190
	s_add_u32 s4, s36, s4
	v_lshlrev_b64 v[4:5], 21, v[190:191]
	s_addc_u32 s5, s37, s5
	v_lshl_add_u64 v[194:195], s[4:5], 0, v[4:5]
	s_mov_b64 s[4:5], 0x100
	v_cndmask_b32_e64 v229, v2, v194, s[0:1]
	v_lshl_add_u64 v[196:197], v[2:3], 0, s[4:5]
	v_mov_b32_e32 v2, 0
	v_cndmask_b32_e64 v191, v3, v195, s[0:1]
	v_add_u32_e32 v230, -1, v193
	v_add_u32_e32 v231, 0x80, v227
	s_mov_b32 s23, -2
	s_mov_b64 s[26:27], 0
	v_mov_b32_e32 v3, v2
	v_mov_b64_e32 v[4:5], 0
	v_mov_b64_e32 v[6:7], 0
	v_mov_b64_e32 v[8:9], 0
	v_mov_b64_e32 v[18:19], 0
	v_mov_b64_e32 v[20:21], 0
	v_mov_b64_e32 v[22:23], 0
	v_mov_b64_e32 v[24:25], 0
	v_mov_b64_e32 v[34:35], 0
	v_mov_b64_e32 v[36:37], 0
	v_mov_b64_e32 v[38:39], 0
	v_mov_b64_e32 v[40:41], 0
	v_mov_b64_e32 v[50:51], 0
	v_mov_b64_e32 v[52:53], 0
	v_mov_b64_e32 v[54:55], 0
	v_mov_b64_e32 v[56:57], 0
	v_mov_b64_e32 v[10:11], 0
	v_mov_b64_e32 v[12:13], 0
	v_mov_b64_e32 v[14:15], 0
	v_mov_b64_e32 v[16:17], 0
	v_mov_b64_e32 v[26:27], 0
	v_mov_b64_e32 v[28:29], 0
	v_mov_b64_e32 v[30:31], 0
	v_mov_b64_e32 v[32:33], 0
	v_mov_b64_e32 v[42:43], 0
	v_mov_b64_e32 v[44:45], 0
	v_mov_b64_e32 v[46:47], 0
	v_mov_b64_e32 v[48:49], 0
	v_mov_b64_e32 v[58:59], 0
	v_mov_b64_e32 v[60:61], 0
	v_mov_b64_e32 v[62:63], 0
	v_mov_b64_e32 v[64:65], 0
	v_mov_b64_e32 v[66:67], 0
	v_mov_b64_e32 v[68:69], 0
	v_mov_b64_e32 v[70:71], 0
	v_mov_b64_e32 v[72:73], 0
	v_mov_b64_e32 v[74:75], 0
	v_mov_b64_e32 v[76:77], 0
	v_mov_b64_e32 v[78:79], 0
	v_mov_b64_e32 v[80:81], 0
	v_mov_b64_e32 v[82:83], 0
	v_mov_b64_e32 v[84:85], 0
	v_mov_b64_e32 v[86:87], 0
	v_mov_b64_e32 v[88:89], 0
	v_mov_b64_e32 v[98:99], 0
	v_mov_b64_e32 v[100:101], 0
	v_mov_b64_e32 v[102:103], 0
	v_mov_b64_e32 v[104:105], 0
	v_mov_b64_e32 v[90:91], 0
	v_mov_b64_e32 v[92:93], 0
	v_mov_b64_e32 v[94:95], 0
	v_mov_b64_e32 v[96:97], 0
	v_mov_b64_e32 v[106:107], 0
	v_mov_b64_e32 v[108:109], 0
	v_mov_b64_e32 v[110:111], 0
	v_mov_b64_e32 v[112:113], 0
	v_mov_b64_e32 v[114:115], 0
	v_mov_b64_e32 v[116:117], 0
	v_mov_b64_e32 v[118:119], 0
	v_mov_b64_e32 v[120:121], 0
	v_mov_b64_e32 v[122:123], 0
	v_mov_b64_e32 v[124:125], 0
	v_mov_b64_e32 v[126:127], 0
	v_mov_b64_e32 v[128:129], 0
	s_cmp_lt_u32 s74, 0x100
	s_cbranch_scc0 .Lzb2
	s_setprio 0
	s_branch .Lz2

; template <class Epi, class Sched>
; __device__ __forceinline__ void gemm_phase(LAS unsigned char* lds, const bf16_t* Abase, const int K, const Sched& S, const Epi& E, const int wvid) {
;     ...
; #pragma unroll
;         for (int a = 0; a < 2; ++a)
; #pragma unroll
;             for (int b = 0; b < 2; ++b)
; #pragma unroll
;                 for (int m = 0; m < 4; ++m)
; #pragma unroll
;                     for (int n = 0; n < 2; ++n) acc[a][b][m][n] = (f32x4){0.f, 0.f, 0.f, 0.f};
.LBB0_1475:
	s_ashr_i32 s25, s24, 31
	s_lshl_b64 s[4:5], s[24:25], 18
	v_ashrrev_i32_e32 v191, 31, v190
	s_add_u32 s4, s36, s4
	v_lshlrev_b64 v[4:5], 20, v[190:191]
	s_addc_u32 s5, s37, s5
	v_lshl_add_u64 v[194:195], s[4:5], 0, v[4:5]
	s_mov_b64 s[4:5], 0x100
	v_cndmask_b32_e64 v229, v2, v194, s[0:1]
	v_lshl_add_u64 v[196:197], v[2:3], 0, s[4:5]
	v_mov_b32_e32 v2, 0
	v_cndmask_b32_e64 v191, v3, v195, s[0:1]
	v_add_u32_e32 v230, 0x80, v228
	s_mov_b32 s25, -2
	s_mov_b64 s[26:27], 0
	v_mov_b32_e32 v3, v2
	v_mov_b64_e32 v[4:5], 0
	v_mov_b64_e32 v[6:7], 0
	v_mov_b64_e32 v[8:9], 0
	v_mov_b64_e32 v[18:19], 0
	v_mov_b64_e32 v[20:21], 0
	v_mov_b64_e32 v[22:23], 0
	v_mov_b64_e32 v[24:25], 0
	v_mov_b64_e32 v[34:35], 0
	v_mov_b64_e32 v[36:37], 0
	v_mov_b64_e32 v[38:39], 0
	v_mov_b64_e32 v[40:41], 0
	v_mov_b64_e32 v[50:51], 0
	v_mov_b64_e32 v[52:53], 0
	v_mov_b64_e32 v[54:55], 0
	v_mov_b64_e32 v[56:57], 0
	v_mov_b64_e32 v[10:11], 0
	v_mov_b64_e32 v[12:13], 0
	v_mov_b64_e32 v[14:15], 0
	v_mov_b64_e32 v[16:17], 0
	v_mov_b64_e32 v[26:27], 0
	v_mov_b64_e32 v[28:29], 0
	v_mov_b64_e32 v[30:31], 0
	v_mov_b64_e32 v[32:33], 0
	v_mov_b64_e32 v[42:43], 0
	v_mov_b64_e32 v[44:45], 0
	v_mov_b64_e32 v[46:47], 0
	v_mov_b64_e32 v[48:49], 0
	v_mov_b64_e32 v[58:59], 0
	v_mov_b64_e32 v[60:61], 0
	v_mov_b64_e32 v[62:63], 0
	v_mov_b64_e32 v[64:65], 0
	v_mov_b64_e32 v[66:67], 0
	v_mov_b64_e32 v[68:69], 0
	v_mov_b64_e32 v[70:71], 0
	v_mov_b64_e32 v[72:73], 0
	v_mov_b64_e32 v[74:75], 0
	v_mov_b64_e32 v[76:77], 0
	v_mov_b64_e32 v[78:79], 0
	v_mov_b64_e32 v[80:81], 0
	v_mov_b64_e32 v[82:83], 0
	v_mov_b64_e32 v[84:85], 0
	v_mov_b64_e32 v[86:87], 0
	v_mov_b64_e32 v[88:89], 0
	v_mov_b64_e32 v[90:91], 0
	v_mov_b64_e32 v[92:93], 0
	v_mov_b64_e32 v[94:95], 0
	v_mov_b64_e32 v[96:97], 0
	v_mov_b64_e32 v[98:99], 0
	v_mov_b64_e32 v[100:101], 0
	v_mov_b64_e32 v[102:103], 0
	v_mov_b64_e32 v[104:105], 0
	v_mov_b64_e32 v[106:107], 0
	v_mov_b64_e32 v[108:109], 0
	v_mov_b64_e32 v[110:111], 0
	v_mov_b64_e32 v[112:113], 0
	v_mov_b64_e32 v[114:115], 0
	v_mov_b64_e32 v[116:117], 0
	v_mov_b64_e32 v[118:119], 0
	v_mov_b64_e32 v[120:121], 0
	v_mov_b64_e32 v[122:123], 0
	v_mov_b64_e32 v[124:125], 0
	v_mov_b64_e32 v[126:127], 0
	v_mov_b64_e32 v[128:129], 0
	s_cmp_lt_u32 s74, 0x100
	s_cbranch_scc0 .Lzb3
	s_setprio 0
	s_branch .Lz3

;     __device__ __forceinline__ void operator()(const f32x4 (&acc)[2][2][4][2], const Unit& u, int wr, int wc, int fr, int fq) const {
;     ...
;         float gt[2][4];
; #pragma unroll
;         for (int ai = 0; ai < 2; ++ai)
; #pragma unroll
;             for (int m = 0; m < 4; ++m) gt[ai][m] = gate[u.loff + min(row0 + ai * HALF + m * 16, u.rend - 1)];
.Lg2x:
	v_add_u32_e32 v160, v227, v178
	v_add_u32_e32 v133, -1, v179
	v_add_u32_e32 v158, 16, v160
	v_min_i32_e32 v130, v158, v133
	v_add_u32_e32 v130, v226, v130
	v_ashrrev_i32_e32 v131, 31, v130
	v_lshl_add_u64 v[130:131], v[130:131], 2, s[20:21]
	v_add_u32_e32 v154, 32, v160
	global_load_dword v156, v[130:131], off
	v_min_i32_e32 v130, v154, v133
	v_add_u32_e32 v130, v226, v130
	v_ashrrev_i32_e32 v131, 31, v130
	v_lshl_add_u64 v[130:131], v[130:131], 2, s[20:21]
	v_add_u32_e32 v150, 48, v160
	global_load_dword v152, v[130:131], off
	v_min_i32_e32 v130, v150, v133
	v_add_u32_e32 v130, v226, v130
	v_ashrrev_i32_e32 v131, 31, v130
	v_lshl_add_u64 v[130:131], v[130:131], 2, s[20:21]
	v_add_u32_e32 v146, 0x80, v160
	global_load_dword v148, v[130:131], off
	v_min_i32_e32 v130, v146, v133
	v_add_u32_e32 v130, v226, v130
	v_ashrrev_i32_e32 v131, 31, v130
	v_lshl_add_u64 v[130:131], v[130:131], 2, s[20:21]
	v_add_u32_e32 v142, 0x90, v160
	global_load_dword v144, v[130:131], off
	v_min_i32_e32 v130, v142, v133
	v_add_u32_e32 v130, v226, v130
	v_ashrrev_i32_e32 v131, 31, v130
	v_lshl_add_u64 v[130:131], v[130:131], 2, s[20:21]
	v_add_u32_e32 v138, 0xa0, v160
	global_load_dword v140, v[130:131], off
	v_min_i32_e32 v130, v138, v133
	v_add_u32_e32 v130, v226, v130
	v_ashrrev_i32_e32 v131, 31, v130
	v_lshl_add_u64 v[130:131], v[130:131], 2, s[20:21]
	v_add_u32_e32 v132, 0xb0, v160
	global_load_dword v134, v[130:131], off
	v_min_i32_e32 v130, v132, v133
	v_add_u32_e32 v130, v226, v130
	v_ashrrev_i32_e32 v131, 31, v130
	v_lshl_add_u64 v[130:131], v[130:131], 2, s[20:21]
	global_load_dword v130, v[130:131], off
	s_cmp_lt_u32 s74, 0x100
	s_cbranch_scc0 .Lxa2
	s_barrier
	s_setprio 2
